# v042 + flattened grid-seam release: last XCD leader bumps all XGEN words, other leaders wait on their own XGEN
# baseline (speedup 1.0000x reference)
; __device__ __forceinline__ unsigned xb_ld(unsigned* p)              { return __hip_atomic_load(p, __ATOMIC_RELAXED, __HIP_MEMORY_SCOPE_AGENT); }
; __device__ __forceinline__ unsigned xb_add(unsigned* p, unsigned v) { return __hip_atomic_fetch_add(p, v, __ATOMIC_RELAXED, __HIP_MEMORY_SCOPE_AGENT); }
; #define XB_SPIN(cond, bar) do { unsigned _sp = 0; while (cond) { __builtin_amdgcn_s_sleep(1); \
;     if ((++_sp & 255u) == 0u) { if (xb_ld(&(bar)[XB_TMO])) break; if (_sp > XB_SPIN_CAP) { atomicAdd(&(bar)[XB_TMO], 1u); break; } } } } while (0)
; __device__ __forceinline__ void xcd_barrier(const XcdBarrier& b) {
;     ...
;         const unsigned old = xb_add(&bar[XB_XSUB(b.x)], 1u);
;         const unsigned gen = old / nloc;
;         if (old + 1u == (gen + 1u) * nloc) {
;             __builtin_amdgcn_fence(__ATOMIC_RELEASE, "agent");
;             asm volatile("s_waitcnt vmcnt(0)" ::: "memory");
;             const unsigned og = xb_add(&bar[XB_TOP], 1u);
;             const unsigned tg = og / nx;
;             if (og + 1u == (tg + 1u) * nx) xb_add(&bar[XB_TOPGEN], 1u);
;             else XB_SPIN(xb_ld(&bar[XB_TOPGEN]) == tg, bar);
.LBB0_210:
	s_andn2_saveexec_b64 s[4:5], s[0:1]
	s_cbranch_execz .LBB0_226
	v_mov_b32_e32 v1, s70
	v_add_co_u32_e32 v4, vcc, 0x7000, v1
	v_mov_b32_e32 v1, s71
	buffer_wbl2 sc1
	s_waitcnt vmcnt(0)
	v_addc_co_u32_e32 v5, vcc, 0, v1, vcc
	v_mov_b32_e32 v1, 1
	flat_atomic_add v1, v[4:5], v1 offset:1024 sc0
	v_cvt_f32_u32_e32 v3, v2
	v_sub_u32_e32 v4, 0, v2
	s_add_u32 s0, s70, 0x7500
	s_addc_u32 s1, s71, 0
	s_add_u32 s100, s25, 0x2400
	s_addc_u32 s101, s24, 0
	v_rcp_iflag_f32_e32 v3, v3
	s_mov_b64 s[8:9], -1
	v_mul_f32_e32 v3, 0x4f7ffffe, v3
	v_cvt_u32_f32_e32 v3, v3
	v_mul_lo_u32 v4, v4, v3
	v_mul_hi_u32 v4, v3, v4
	v_add_u32_e32 v3, v3, v4
	s_waitcnt vmcnt(0) lgkmcnt(0)
	v_mul_hi_u32 v3, v1, v3
	v_mul_lo_u32 v5, v3, v2
	v_add_u32_e32 v4, 1, v1
	v_sub_u32_e32 v1, v1, v5
	v_add_u32_e32 v6, 1, v3
	v_cmp_ge_u32_e32 vcc, v1, v2
	v_sub_u32_e32 v5, v1, v2
	s_nop 0
	v_cndmask_b32_e32 v3, v3, v6, vcc
	v_cndmask_b32_e32 v1, v1, v5, vcc
	v_add_u32_e32 v5, 1, v3
	v_cmp_ge_u32_e32 vcc, v1, v2
	s_nop 1
	v_cndmask_b32_e32 v1, v3, v5, vcc
	v_mad_u64_u32 v[2:3], s[6:7], v2, v1, v[2:3]
	v_cmp_ne_u32_e32 vcc, v4, v2
	v_mov_b64_e32 v[2:3], s[0:1]
	s_and_saveexec_b64 s[6:7], vcc
	s_cbranch_execz .LBB0_223
	v_mov_b64_e32 v[2:3], s[100:101]
	flat_load_dword v2, v[2:3] sc1
	s_mov_b64 s[12:13], 0
	s_waitcnt vmcnt(0) lgkmcnt(0)
	v_cmp_eq_u32_e32 vcc, v2, v1
	s_and_saveexec_b64 s[10:11], vcc
	s_cbranch_execz .LBB0_222
	s_add_u32 s8, s70, 0x4200
	s_addc_u32 s9, s71, 0
	s_mov_b32 s26, 1
	s_branch .LBB0_215

; __device__ __forceinline__ unsigned xb_ld(unsigned* p)              { return __hip_atomic_load(p, __ATOMIC_RELAXED, __HIP_MEMORY_SCOPE_AGENT); }
; #define XB_SPIN(cond, bar) do { unsigned _sp = 0; while (cond) { __builtin_amdgcn_s_sleep(1); \
;     if ((++_sp & 255u) == 0u) { if (xb_ld(&(bar)[XB_TMO])) break; if (_sp > XB_SPIN_CAP) { atomicAdd(&(bar)[XB_TMO], 1u); break; } } } } while (0)
; __device__ __forceinline__ void xcd_barrier(const XcdBarrier& b) {
;     ...
;             else XB_SPIN(xb_ld(&bar[XB_TOPGEN]) == tg, bar);
.LBB0_220:
	v_mov_b64_e32 v[2:3], s[100:101]
	flat_load_dword v2, v[2:3] sc1
	s_add_i32 s26, s26, 1
	s_or_b64 s[16:17], s[16:17], exec
	s_waitcnt vmcnt(0) lgkmcnt(0)
	v_cmp_ne_u32_e32 vcc, v2, v1
	s_orn2_b64 s[20:21], vcc, exec
	s_branch .LBB0_214

; __device__ __forceinline__ unsigned xb_ld(unsigned* p)              { return __hip_atomic_load(p, __ATOMIC_RELAXED, __HIP_MEMORY_SCOPE_AGENT); }
; __device__ __forceinline__ unsigned xb_add(unsigned* p, unsigned v) { return __hip_atomic_fetch_add(p, v, __ATOMIC_RELAXED, __HIP_MEMORY_SCOPE_AGENT); }
; #define XB_SPIN(cond, bar) do { unsigned _sp = 0; while (cond) { __builtin_amdgcn_s_sleep(1); \
;     if ((++_sp & 255u) == 0u) { if (xb_ld(&(bar)[XB_TMO])) break; if (_sp > XB_SPIN_CAP) { atomicAdd(&(bar)[XB_TMO], 1u); break; } } } } while (0)
; __device__ __forceinline__ void xcd_barrier(const XcdBarrier& b) {
;     ...
;             if (og + 1u == (tg + 1u) * nx) xb_add(&bar[XB_TOPGEN], 1u);
;             else XB_SPIN(xb_ld(&bar[XB_TOPGEN]) == tg, bar);
;             __builtin_amdgcn_fence(__ATOMIC_ACQUIRE, "agent");
;             xb_add(&bar[XB_XGEN(b.x)], 1u);
.LBB0_223:
	s_or_b64 exec, exec, s[6:7]
	s_and_saveexec_b64 s[0:1], s[8:9]
	s_cbranch_execz .LBB0_225
	v_mov_b32_e32 v1, 1
	flat_atomic_add v[2:3], v1
	v_mov_b32_e32 v4, s70
	v_add_co_u32_e32 v4, vcc, 0x6000, v4
	v_mov_b32_e32 v5, s71
	s_nop 0
	v_addc_co_u32_e32 v5, vcc, 0, v5, vcc
	flat_atomic_add v[4:5], v1 offset:1024
	flat_atomic_add v[4:5], v1 offset:1280
	flat_atomic_add v[4:5], v1 offset:1536
	flat_atomic_add v[4:5], v1 offset:1792
	flat_atomic_add v[4:5], v1 offset:2048
	flat_atomic_add v[4:5], v1 offset:2304
	flat_atomic_add v[4:5], v1 offset:2560
	flat_atomic_add v[4:5], v1 offset:2816
.LBB0_225:
	s_or_b64 exec, exec, s[0:1]
	v_mov_b32_e32 v1, s25
	v_add_co_u32_e32 v2, vcc, 0x2000, v1
	v_mov_b32_e32 v1, s24
	s_nop 0
	v_addc_co_u32_e32 v3, vcc, 0, v1, vcc
	v_mov_b32_e32 v1, 1
	s_waitcnt vmcnt(0) lgkmcnt(0)
	buffer_inv sc1
	s_waitcnt vmcnt(0)

; __device__ __forceinline__ unsigned xb_ld(unsigned* p)              { return __hip_atomic_load(p, __ATOMIC_RELAXED, __HIP_MEMORY_SCOPE_AGENT); }
; __device__ __forceinline__ unsigned xb_add(unsigned* p, unsigned v) { return __hip_atomic_fetch_add(p, v, __ATOMIC_RELAXED, __HIP_MEMORY_SCOPE_AGENT); }
; #define XB_SPIN(cond, bar) do { unsigned _sp = 0; while (cond) { __builtin_amdgcn_s_sleep(1); \
;     if ((++_sp & 255u) == 0u) { if (xb_ld(&(bar)[XB_TMO])) break; if (_sp > XB_SPIN_CAP) { atomicAdd(&(bar)[XB_TMO], 1u); break; } } } } while (0)
; __device__ __forceinline__ void xcd_barrier(const XcdBarrier& b) {
;     ...
;         const unsigned old = xb_add(&bar[XB_XSUB(b.x)], 1u);
;         const unsigned gen = old / nloc;
;         if (old + 1u == (gen + 1u) * nloc) {
;             __builtin_amdgcn_fence(__ATOMIC_RELEASE, "agent");
;             asm volatile("s_waitcnt vmcnt(0)" ::: "memory");
;             const unsigned og = xb_add(&bar[XB_TOP], 1u);
;             const unsigned tg = og / nx;
;             if (og + 1u == (tg + 1u) * nx) xb_add(&bar[XB_TOPGEN], 1u);
;             else XB_SPIN(xb_ld(&bar[XB_TOPGEN]) == tg, bar);
.LBB0_268:
	s_andn2_saveexec_b64 s[4:5], s[0:1]
	s_cbranch_execz .LBB0_284
	v_mov_b32_e32 v1, s33
	v_add_co_u32_e32 v4, vcc, 0x7000, v1
	v_mov_b32_e32 v1, s38
	buffer_wbl2 sc1
	s_waitcnt vmcnt(0)
	v_addc_co_u32_e32 v5, vcc, 0, v1, vcc
	v_mov_b32_e32 v1, 1
	flat_atomic_add v1, v[4:5], v1 offset:1024 sc0
	v_cvt_f32_u32_e32 v3, v2
	v_sub_u32_e32 v4, 0, v2
	s_add_u32 s0, s33, 0x7500
	s_addc_u32 s1, s38, 0
	s_add_u32 s100, s25, 0x2400
	s_addc_u32 s101, s24, 0
	v_rcp_iflag_f32_e32 v3, v3
	s_mov_b64 s[8:9], -1
	v_mul_f32_e32 v3, 0x4f7ffffe, v3
	v_cvt_u32_f32_e32 v3, v3
	v_mul_lo_u32 v4, v4, v3
	v_mul_hi_u32 v4, v3, v4
	v_add_u32_e32 v3, v3, v4
	s_waitcnt vmcnt(0) lgkmcnt(0)
	v_mul_hi_u32 v3, v1, v3
	v_mul_lo_u32 v5, v3, v2
	v_add_u32_e32 v4, 1, v1
	v_sub_u32_e32 v1, v1, v5
	v_add_u32_e32 v6, 1, v3
	v_cmp_ge_u32_e32 vcc, v1, v2
	v_sub_u32_e32 v5, v1, v2
	s_nop 0
	v_cndmask_b32_e32 v3, v3, v6, vcc
	v_cndmask_b32_e32 v1, v1, v5, vcc
	v_add_u32_e32 v5, 1, v3
	v_cmp_ge_u32_e32 vcc, v1, v2
	s_nop 1
	v_cndmask_b32_e32 v1, v3, v5, vcc
	v_mad_u64_u32 v[2:3], s[6:7], v2, v1, v[2:3]
	v_cmp_ne_u32_e32 vcc, v4, v2
	v_mov_b64_e32 v[2:3], s[0:1]
	s_and_saveexec_b64 s[6:7], vcc
	s_cbranch_execz .LBB0_281
	v_mov_b64_e32 v[2:3], s[100:101]
	flat_load_dword v2, v[2:3] sc1
	s_mov_b64 s[12:13], 0
	s_waitcnt vmcnt(0) lgkmcnt(0)
	v_cmp_eq_u32_e32 vcc, v2, v1
	s_and_saveexec_b64 s[10:11], vcc
	s_cbranch_execz .LBB0_280
	s_add_u32 s8, s33, 0x4200
	s_addc_u32 s9, s38, 0
	s_mov_b32 s26, 1
	s_branch .LBB0_273

; __device__ __forceinline__ unsigned xb_ld(unsigned* p)              { return __hip_atomic_load(p, __ATOMIC_RELAXED, __HIP_MEMORY_SCOPE_AGENT); }
; __device__ __forceinline__ unsigned xb_add(unsigned* p, unsigned v) { return __hip_atomic_fetch_add(p, v, __ATOMIC_RELAXED, __HIP_MEMORY_SCOPE_AGENT); }
; #define XB_SPIN(cond, bar) do { unsigned _sp = 0; while (cond) { __builtin_amdgcn_s_sleep(1); \
;     if ((++_sp & 255u) == 0u) { if (xb_ld(&(bar)[XB_TMO])) break; if (_sp > XB_SPIN_CAP) { atomicAdd(&(bar)[XB_TMO], 1u); break; } } } } while (0)
; __device__ __forceinline__ void xcd_barrier(const XcdBarrier& b) {
;     ...
;             if (og + 1u == (tg + 1u) * nx) xb_add(&bar[XB_TOPGEN], 1u);
;             else XB_SPIN(xb_ld(&bar[XB_TOPGEN]) == tg, bar);
;             __builtin_amdgcn_fence(__ATOMIC_ACQUIRE, "agent");
;             xb_add(&bar[XB_XGEN(b.x)], 1u);
.LBB0_281:
	s_or_b64 exec, exec, s[6:7]
	s_and_saveexec_b64 s[0:1], s[8:9]
	s_cbranch_execz .LBB0_283
	v_mov_b32_e32 v1, 1
	flat_atomic_add v[2:3], v1
	v_mov_b32_e32 v4, s33
	v_add_co_u32_e32 v4, vcc, 0x6000, v4
	v_mov_b32_e32 v5, s38
	s_nop 0
	v_addc_co_u32_e32 v5, vcc, 0, v5, vcc
	flat_atomic_add v[4:5], v1 offset:1024
	flat_atomic_add v[4:5], v1 offset:1280
	flat_atomic_add v[4:5], v1 offset:1536
	flat_atomic_add v[4:5], v1 offset:1792
	flat_atomic_add v[4:5], v1 offset:2048
	flat_atomic_add v[4:5], v1 offset:2304
	flat_atomic_add v[4:5], v1 offset:2560
	flat_atomic_add v[4:5], v1 offset:2816

; __device__ __forceinline__ unsigned xb_ld(unsigned* p)              { return __hip_atomic_load(p, __ATOMIC_RELAXED, __HIP_MEMORY_SCOPE_AGENT); }
; __device__ __forceinline__ unsigned xb_add(unsigned* p, unsigned v) { return __hip_atomic_fetch_add(p, v, __ATOMIC_RELAXED, __HIP_MEMORY_SCOPE_AGENT); }
; #define XB_SPIN(cond, bar) do { unsigned _sp = 0; while (cond) { __builtin_amdgcn_s_sleep(1); \
;     if ((++_sp & 255u) == 0u) { if (xb_ld(&(bar)[XB_TMO])) break; if (_sp > XB_SPIN_CAP) { atomicAdd(&(bar)[XB_TMO], 1u); break; } } } } while (0)
; __device__ __forceinline__ void xcd_barrier(const XcdBarrier& b) {
;     ...
;         const unsigned old = xb_add(&bar[XB_XSUB(b.x)], 1u);
;         const unsigned gen = old / nloc;
;         if (old + 1u == (gen + 1u) * nloc) {
;             __builtin_amdgcn_fence(__ATOMIC_RELEASE, "agent");
;             asm volatile("s_waitcnt vmcnt(0)" ::: "memory");
;             const unsigned og = xb_add(&bar[XB_TOP], 1u);
;             const unsigned tg = og / nx;
;             if (og + 1u == (tg + 1u) * nx) xb_add(&bar[XB_TOPGEN], 1u);
;             else XB_SPIN(xb_ld(&bar[XB_TOPGEN]) == tg, bar);
.LBB0_401:
	s_andn2_saveexec_b64 s[4:5], s[0:1]
	s_cbranch_execz .LBB0_417
	v_mov_b32_e32 v1, s38
	v_add_co_u32_e32 v4, vcc, 0x7000, v1
	v_mov_b32_e32 v1, s39
	buffer_wbl2 sc1
	s_waitcnt vmcnt(0)
	v_addc_co_u32_e32 v5, vcc, 0, v1, vcc
	v_mov_b32_e32 v1, 1
	flat_atomic_add v1, v[4:5], v1 offset:1024 sc0
	v_cvt_f32_u32_e32 v3, v2
	v_sub_u32_e32 v4, 0, v2
	s_add_u32 s0, s38, 0x7500
	s_addc_u32 s1, s39, 0
	s_add_u32 s100, s25, 0x2400
	s_addc_u32 s101, s24, 0
	v_rcp_iflag_f32_e32 v3, v3
	s_mov_b64 s[8:9], -1
	v_mul_f32_e32 v3, 0x4f7ffffe, v3
	v_cvt_u32_f32_e32 v3, v3
	v_mul_lo_u32 v4, v4, v3
	v_mul_hi_u32 v4, v3, v4
	v_add_u32_e32 v3, v3, v4
	s_waitcnt vmcnt(0) lgkmcnt(0)
	v_mul_hi_u32 v3, v1, v3
	v_mul_lo_u32 v5, v3, v2
	v_add_u32_e32 v4, 1, v1
	v_sub_u32_e32 v1, v1, v5
	v_add_u32_e32 v6, 1, v3
	v_cmp_ge_u32_e32 vcc, v1, v2
	v_sub_u32_e32 v5, v1, v2
	s_nop 0
	v_cndmask_b32_e32 v3, v3, v6, vcc
	v_cndmask_b32_e32 v1, v1, v5, vcc
	v_add_u32_e32 v5, 1, v3
	v_cmp_ge_u32_e32 vcc, v1, v2
	s_nop 1
	v_cndmask_b32_e32 v1, v3, v5, vcc
	v_mad_u64_u32 v[2:3], s[6:7], v2, v1, v[2:3]
	v_cmp_ne_u32_e32 vcc, v4, v2
	v_mov_b64_e32 v[2:3], s[0:1]
	s_and_saveexec_b64 s[6:7], vcc
	s_cbranch_execz .LBB0_414
	v_mov_b64_e32 v[2:3], s[100:101]
	flat_load_dword v2, v[2:3] sc1
	s_mov_b64 s[12:13], 0
	s_waitcnt vmcnt(0) lgkmcnt(0)
	v_cmp_eq_u32_e32 vcc, v2, v1
	s_and_saveexec_b64 s[10:11], vcc
	s_cbranch_execz .LBB0_413
	s_add_u32 s8, s38, 0x4200
	s_addc_u32 s9, s39, 0
	s_mov_b32 s26, 1
	s_branch .LBB0_406

; __device__ __forceinline__ unsigned xb_ld(unsigned* p)              { return __hip_atomic_load(p, __ATOMIC_RELAXED, __HIP_MEMORY_SCOPE_AGENT); }
; __device__ __forceinline__ unsigned xb_add(unsigned* p, unsigned v) { return __hip_atomic_fetch_add(p, v, __ATOMIC_RELAXED, __HIP_MEMORY_SCOPE_AGENT); }
; #define XB_SPIN(cond, bar) do { unsigned _sp = 0; while (cond) { __builtin_amdgcn_s_sleep(1); \
;     if ((++_sp & 255u) == 0u) { if (xb_ld(&(bar)[XB_TMO])) break; if (_sp > XB_SPIN_CAP) { atomicAdd(&(bar)[XB_TMO], 1u); break; } } } } while (0)
; __device__ __forceinline__ void xcd_barrier(const XcdBarrier& b) {
;     ...
;             if (og + 1u == (tg + 1u) * nx) xb_add(&bar[XB_TOPGEN], 1u);
;             else XB_SPIN(xb_ld(&bar[XB_TOPGEN]) == tg, bar);
;             __builtin_amdgcn_fence(__ATOMIC_ACQUIRE, "agent");
;             xb_add(&bar[XB_XGEN(b.x)], 1u);
.LBB0_414:
	s_or_b64 exec, exec, s[6:7]
	s_and_saveexec_b64 s[0:1], s[8:9]
	s_cbranch_execz .LBB0_416
	v_mov_b32_e32 v1, 1
	flat_atomic_add v[2:3], v1
	v_mov_b32_e32 v4, s38
	v_add_co_u32_e32 v4, vcc, 0x6000, v4
	v_mov_b32_e32 v5, s39
	s_nop 0
	v_addc_co_u32_e32 v5, vcc, 0, v5, vcc
	flat_atomic_add v[4:5], v1 offset:1024
	flat_atomic_add v[4:5], v1 offset:1280
	flat_atomic_add v[4:5], v1 offset:1536
	flat_atomic_add v[4:5], v1 offset:1792
	flat_atomic_add v[4:5], v1 offset:2048
	flat_atomic_add v[4:5], v1 offset:2304
	flat_atomic_add v[4:5], v1 offset:2560
	flat_atomic_add v[4:5], v1 offset:2816

; __device__ __forceinline__ unsigned xb_ld(unsigned* p)              { return __hip_atomic_load(p, __ATOMIC_RELAXED, __HIP_MEMORY_SCOPE_AGENT); }
; __device__ __forceinline__ unsigned xb_add(unsigned* p, unsigned v) { return __hip_atomic_fetch_add(p, v, __ATOMIC_RELAXED, __HIP_MEMORY_SCOPE_AGENT); }
; #define XB_SPIN(cond, bar) do { unsigned _sp = 0; while (cond) { __builtin_amdgcn_s_sleep(1); \
;     if ((++_sp & 255u) == 0u) { if (xb_ld(&(bar)[XB_TMO])) break; if (_sp > XB_SPIN_CAP) { atomicAdd(&(bar)[XB_TMO], 1u); break; } } } } while (0)
; __device__ __forceinline__ void xcd_barrier(const XcdBarrier& b) {
;     ...
;         const unsigned old = xb_add(&bar[XB_XSUB(b.x)], 1u);
;         const unsigned gen = old / nloc;
;         if (old + 1u == (gen + 1u) * nloc) {
;             __builtin_amdgcn_fence(__ATOMIC_RELEASE, "agent");
;             asm volatile("s_waitcnt vmcnt(0)" ::: "memory");
;             const unsigned og = xb_add(&bar[XB_TOP], 1u);
;             const unsigned tg = og / nx;
;             if (og + 1u == (tg + 1u) * nx) xb_add(&bar[XB_TOPGEN], 1u);
;             else XB_SPIN(xb_ld(&bar[XB_TOPGEN]) == tg, bar);
.LBB0_509:
	s_andn2_saveexec_b64 s[4:5], s[0:1]
	s_cbranch_execz .LBB0_525
	v_mov_b32_e32 v1, s2
	v_add_co_u32_e32 v4, vcc, 0x7000, v1
	v_mov_b32_e32 v1, s3
	buffer_wbl2 sc1
	s_waitcnt vmcnt(0)
	v_addc_co_u32_e32 v5, vcc, 0, v1, vcc
	v_mov_b32_e32 v1, 1
	flat_atomic_add v1, v[4:5], v1 offset:1024 sc0
	v_cvt_f32_u32_e32 v3, v2
	v_sub_u32_e32 v4, 0, v2
	s_add_u32 s0, s2, 0x7500
	s_addc_u32 s1, s3, 0
	s_add_u32 s100, s27, 0x2400
	s_addc_u32 s101, s26, 0
	v_rcp_iflag_f32_e32 v3, v3
	s_mov_b64 s[8:9], -1
	v_mul_f32_e32 v3, 0x4f7ffffe, v3
	v_cvt_u32_f32_e32 v3, v3
	v_mul_lo_u32 v4, v4, v3
	v_mul_hi_u32 v4, v3, v4
	v_add_u32_e32 v3, v3, v4
	s_waitcnt vmcnt(0) lgkmcnt(0)
	v_mul_hi_u32 v3, v1, v3
	v_mul_lo_u32 v5, v3, v2
	v_add_u32_e32 v4, 1, v1
	v_sub_u32_e32 v1, v1, v5
	v_add_u32_e32 v6, 1, v3
	v_cmp_ge_u32_e32 vcc, v1, v2
	v_sub_u32_e32 v5, v1, v2
	s_nop 0
	v_cndmask_b32_e32 v3, v3, v6, vcc
	v_cndmask_b32_e32 v1, v1, v5, vcc
	v_add_u32_e32 v5, 1, v3
	v_cmp_ge_u32_e32 vcc, v1, v2
	s_nop 1
	v_cndmask_b32_e32 v1, v3, v5, vcc
	v_mad_u64_u32 v[2:3], s[6:7], v2, v1, v[2:3]
	v_cmp_ne_u32_e32 vcc, v4, v2
	v_mov_b64_e32 v[2:3], s[0:1]
	s_and_saveexec_b64 s[6:7], vcc
	s_cbranch_execz .LBB0_522
	v_mov_b64_e32 v[2:3], s[100:101]
	flat_load_dword v2, v[2:3] sc1
	s_mov_b64 s[12:13], 0
	s_waitcnt vmcnt(0) lgkmcnt(0)
	v_cmp_eq_u32_e32 vcc, v2, v1
	s_and_saveexec_b64 s[10:11], vcc
	s_cbranch_execz .LBB0_521
	s_add_u32 s8, s2, 0x4200
	s_addc_u32 s9, s3, 0
	s_mov_b32 s28, 1
	s_branch .LBB0_514

; __device__ __forceinline__ unsigned xb_ld(unsigned* p)              { return __hip_atomic_load(p, __ATOMIC_RELAXED, __HIP_MEMORY_SCOPE_AGENT); }
; #define XB_SPIN(cond, bar) do { unsigned _sp = 0; while (cond) { __builtin_amdgcn_s_sleep(1); \
;     if ((++_sp & 255u) == 0u) { if (xb_ld(&(bar)[XB_TMO])) break; if (_sp > XB_SPIN_CAP) { atomicAdd(&(bar)[XB_TMO], 1u); break; } } } } while (0)
; __device__ __forceinline__ void xcd_barrier(const XcdBarrier& b) {
;     ...
;             else XB_SPIN(xb_ld(&bar[XB_TOPGEN]) == tg, bar);
.LBB0_519:
	v_mov_b64_e32 v[2:3], s[100:101]
	flat_load_dword v2, v[2:3] sc1
	s_add_i32 s28, s28, 1
	s_or_b64 s[16:17], s[16:17], exec
	s_waitcnt vmcnt(0) lgkmcnt(0)
	v_cmp_ne_u32_e32 vcc, v2, v1
	s_orn2_b64 s[22:23], vcc, exec
	s_branch .LBB0_513

; __device__ __forceinline__ unsigned xb_ld(unsigned* p)              { return __hip_atomic_load(p, __ATOMIC_RELAXED, __HIP_MEMORY_SCOPE_AGENT); }
; __device__ __forceinline__ unsigned xb_add(unsigned* p, unsigned v) { return __hip_atomic_fetch_add(p, v, __ATOMIC_RELAXED, __HIP_MEMORY_SCOPE_AGENT); }
; #define XB_SPIN(cond, bar) do { unsigned _sp = 0; while (cond) { __builtin_amdgcn_s_sleep(1); \
;     if ((++_sp & 255u) == 0u) { if (xb_ld(&(bar)[XB_TMO])) break; if (_sp > XB_SPIN_CAP) { atomicAdd(&(bar)[XB_TMO], 1u); break; } } } } while (0)
; __device__ __forceinline__ void xcd_barrier(const XcdBarrier& b) {
;     ...
;             if (og + 1u == (tg + 1u) * nx) xb_add(&bar[XB_TOPGEN], 1u);
;             else XB_SPIN(xb_ld(&bar[XB_TOPGEN]) == tg, bar);
;             __builtin_amdgcn_fence(__ATOMIC_ACQUIRE, "agent");
;             xb_add(&bar[XB_XGEN(b.x)], 1u);
.LBB0_522:
	s_or_b64 exec, exec, s[6:7]
	s_and_saveexec_b64 s[0:1], s[8:9]
	s_cbranch_execz .LBB0_524
	v_mov_b32_e32 v1, 1
	flat_atomic_add v[2:3], v1
	v_mov_b32_e32 v4, s2
	v_add_co_u32_e32 v4, vcc, 0x6000, v4
	v_mov_b32_e32 v5, s3
	s_nop 0
	v_addc_co_u32_e32 v5, vcc, 0, v5, vcc
	flat_atomic_add v[4:5], v1 offset:1024
	flat_atomic_add v[4:5], v1 offset:1280
	flat_atomic_add v[4:5], v1 offset:1536
	flat_atomic_add v[4:5], v1 offset:1792
	flat_atomic_add v[4:5], v1 offset:2048
	flat_atomic_add v[4:5], v1 offset:2304
	flat_atomic_add v[4:5], v1 offset:2560
	flat_atomic_add v[4:5], v1 offset:2816
.LBB0_524:
	s_or_b64 exec, exec, s[0:1]
	v_mov_b32_e32 v1, s27
	v_add_co_u32_e32 v2, vcc, 0x2000, v1
	v_mov_b32_e32 v1, s26
	s_nop 0
	v_addc_co_u32_e32 v3, vcc, 0, v1, vcc
	v_mov_b32_e32 v1, 1
	s_waitcnt vmcnt(0) lgkmcnt(0)
	buffer_inv sc1
	s_waitcnt vmcnt(0)

; __device__ __forceinline__ unsigned xb_ld(unsigned* p)              { return __hip_atomic_load(p, __ATOMIC_RELAXED, __HIP_MEMORY_SCOPE_AGENT); }
; __device__ __forceinline__ unsigned xb_add(unsigned* p, unsigned v) { return __hip_atomic_fetch_add(p, v, __ATOMIC_RELAXED, __HIP_MEMORY_SCOPE_AGENT); }
; #define XB_SPIN(cond, bar) do { unsigned _sp = 0; while (cond) { __builtin_amdgcn_s_sleep(1); \
;     if ((++_sp & 255u) == 0u) { if (xb_ld(&(bar)[XB_TMO])) break; if (_sp > XB_SPIN_CAP) { atomicAdd(&(bar)[XB_TMO], 1u); break; } } } } while (0)
; __device__ __forceinline__ void xcd_barrier(const XcdBarrier& b) {
;     ...
;         const unsigned old = xb_add(&bar[XB_XSUB(b.x)], 1u);
;         const unsigned gen = old / nloc;
;         if (old + 1u == (gen + 1u) * nloc) {
;             __builtin_amdgcn_fence(__ATOMIC_RELEASE, "agent");
;             asm volatile("s_waitcnt vmcnt(0)" ::: "memory");
;             const unsigned og = xb_add(&bar[XB_TOP], 1u);
;             const unsigned tg = og / nx;
;             if (og + 1u == (tg + 1u) * nx) xb_add(&bar[XB_TOPGEN], 1u);
;             else XB_SPIN(xb_ld(&bar[XB_TOPGEN]) == tg, bar);
.LBB0_606:
	s_andn2_saveexec_b64 s[4:5], s[0:1]
	s_cbranch_execz .LBB0_622
	v_mov_b32_e32 v1, s47
	v_add_co_u32_e32 v4, vcc, 0x7000, v1
	v_mov_b32_e32 v1, s48
	buffer_wbl2 sc1
	s_waitcnt vmcnt(0)
	v_addc_co_u32_e32 v5, vcc, 0, v1, vcc
	v_mov_b32_e32 v1, 1
	flat_atomic_add v1, v[4:5], v1 offset:1024 sc0
	v_cvt_f32_u32_e32 v3, v2
	v_sub_u32_e32 v4, 0, v2
	s_add_u32 s0, s47, 0x7500
	s_addc_u32 s1, s48, 0
	s_add_u32 s100, s25, 0x2400
	s_addc_u32 s101, s24, 0
	v_rcp_iflag_f32_e32 v3, v3
	s_mov_b64 s[8:9], -1
	v_mul_f32_e32 v3, 0x4f7ffffe, v3
	v_cvt_u32_f32_e32 v3, v3
	v_mul_lo_u32 v4, v4, v3
	v_mul_hi_u32 v4, v3, v4
	v_add_u32_e32 v3, v3, v4
	s_waitcnt vmcnt(0) lgkmcnt(0)
	v_mul_hi_u32 v3, v1, v3
	v_mul_lo_u32 v5, v3, v2
	v_add_u32_e32 v4, 1, v1
	v_sub_u32_e32 v1, v1, v5
	v_add_u32_e32 v6, 1, v3
	v_cmp_ge_u32_e32 vcc, v1, v2
	v_sub_u32_e32 v5, v1, v2
	s_nop 0
	v_cndmask_b32_e32 v3, v3, v6, vcc
	v_cndmask_b32_e32 v1, v1, v5, vcc
	v_add_u32_e32 v5, 1, v3
	v_cmp_ge_u32_e32 vcc, v1, v2
	s_nop 1
	v_cndmask_b32_e32 v1, v3, v5, vcc
	v_mad_u64_u32 v[2:3], s[6:7], v2, v1, v[2:3]
	v_cmp_ne_u32_e32 vcc, v4, v2
	v_mov_b64_e32 v[2:3], s[0:1]
	s_and_saveexec_b64 s[6:7], vcc
	s_cbranch_execz .LBB0_619
	v_mov_b64_e32 v[2:3], s[100:101]
	flat_load_dword v2, v[2:3] sc1
	s_mov_b64 s[12:13], 0
	s_waitcnt vmcnt(0) lgkmcnt(0)
	v_cmp_eq_u32_e32 vcc, v2, v1
	s_and_saveexec_b64 s[10:11], vcc
	s_cbranch_execz .LBB0_618
	s_add_u32 s8, s47, 0x4200
	s_addc_u32 s9, s48, 0
	s_mov_b32 s26, 1
	s_branch .LBB0_611

; __device__ __forceinline__ unsigned xb_ld(unsigned* p)              { return __hip_atomic_load(p, __ATOMIC_RELAXED, __HIP_MEMORY_SCOPE_AGENT); }
; __device__ __forceinline__ unsigned xb_add(unsigned* p, unsigned v) { return __hip_atomic_fetch_add(p, v, __ATOMIC_RELAXED, __HIP_MEMORY_SCOPE_AGENT); }
; #define XB_SPIN(cond, bar) do { unsigned _sp = 0; while (cond) { __builtin_amdgcn_s_sleep(1); \
;     if ((++_sp & 255u) == 0u) { if (xb_ld(&(bar)[XB_TMO])) break; if (_sp > XB_SPIN_CAP) { atomicAdd(&(bar)[XB_TMO], 1u); break; } } } } while (0)
; __device__ __forceinline__ void xcd_barrier(const XcdBarrier& b) {
;     ...
;             if (og + 1u == (tg + 1u) * nx) xb_add(&bar[XB_TOPGEN], 1u);
;             else XB_SPIN(xb_ld(&bar[XB_TOPGEN]) == tg, bar);
;             __builtin_amdgcn_fence(__ATOMIC_ACQUIRE, "agent");
;             xb_add(&bar[XB_XGEN(b.x)], 1u);
.LBB0_619:
	s_or_b64 exec, exec, s[6:7]
	s_and_saveexec_b64 s[0:1], s[8:9]
	s_cbranch_execz .LBB0_621
	v_mov_b32_e32 v1, 1
	flat_atomic_add v[2:3], v1
	v_mov_b32_e32 v4, s47
	v_add_co_u32_e32 v4, vcc, 0x6000, v4
	v_mov_b32_e32 v5, s48
	s_nop 0
	v_addc_co_u32_e32 v5, vcc, 0, v5, vcc
	flat_atomic_add v[4:5], v1 offset:1024
	flat_atomic_add v[4:5], v1 offset:1280
	flat_atomic_add v[4:5], v1 offset:1536
	flat_atomic_add v[4:5], v1 offset:1792
	flat_atomic_add v[4:5], v1 offset:2048
	flat_atomic_add v[4:5], v1 offset:2304
	flat_atomic_add v[4:5], v1 offset:2560
	flat_atomic_add v[4:5], v1 offset:2816

; __device__ __forceinline__ unsigned xb_ld(unsigned* p)              { return __hip_atomic_load(p, __ATOMIC_RELAXED, __HIP_MEMORY_SCOPE_AGENT); }
; __device__ __forceinline__ unsigned xb_add(unsigned* p, unsigned v) { return __hip_atomic_fetch_add(p, v, __ATOMIC_RELAXED, __HIP_MEMORY_SCOPE_AGENT); }
; #define XB_SPIN(cond, bar) do { unsigned _sp = 0; while (cond) { __builtin_amdgcn_s_sleep(1); \
;     if ((++_sp & 255u) == 0u) { if (xb_ld(&(bar)[XB_TMO])) break; if (_sp > XB_SPIN_CAP) { atomicAdd(&(bar)[XB_TMO], 1u); break; } } } } while (0)
; __device__ __forceinline__ void xcd_barrier(const XcdBarrier& b) {
;     ...
;         const unsigned old = xb_add(&bar[XB_XSUB(b.x)], 1u);
;         const unsigned gen = old / nloc;
;         if (old + 1u == (gen + 1u) * nloc) {
;             __builtin_amdgcn_fence(__ATOMIC_RELEASE, "agent");
;             asm volatile("s_waitcnt vmcnt(0)" ::: "memory");
;             const unsigned og = xb_add(&bar[XB_TOP], 1u);
;             const unsigned tg = og / nx;
;             if (og + 1u == (tg + 1u) * nx) xb_add(&bar[XB_TOPGEN], 1u);
;             else XB_SPIN(xb_ld(&bar[XB_TOPGEN]) == tg, bar);
.LBB0_763:
	s_andn2_saveexec_b64 s[4:5], s[0:1]
	s_cbranch_execz .LBB0_779
	v_mov_b32_e32 v1, s42
	v_add_co_u32_e32 v4, vcc, 0x7000, v1
	v_mov_b32_e32 v1, s43
	buffer_wbl2 sc1
	s_waitcnt vmcnt(0)
	v_addc_co_u32_e32 v5, vcc, 0, v1, vcc
	v_mov_b32_e32 v1, 1
	flat_atomic_add v1, v[4:5], v1 offset:1024 sc0
	v_cvt_f32_u32_e32 v3, v2
	v_sub_u32_e32 v4, 0, v2
	s_add_u32 s0, s42, 0x7500
	s_addc_u32 s1, s43, 0
	s_add_u32 s100, s25, 0x2400
	s_addc_u32 s101, s24, 0
	v_rcp_iflag_f32_e32 v3, v3
	s_mov_b64 s[8:9], -1
	v_mul_f32_e32 v3, 0x4f7ffffe, v3
	v_cvt_u32_f32_e32 v3, v3
	v_mul_lo_u32 v4, v4, v3
	v_mul_hi_u32 v4, v3, v4
	v_add_u32_e32 v3, v3, v4
	s_waitcnt vmcnt(0) lgkmcnt(0)
	v_mul_hi_u32 v3, v1, v3
	v_mul_lo_u32 v5, v3, v2
	v_add_u32_e32 v4, 1, v1
	v_sub_u32_e32 v1, v1, v5
	v_add_u32_e32 v6, 1, v3
	v_cmp_ge_u32_e32 vcc, v1, v2
	v_sub_u32_e32 v5, v1, v2
	s_nop 0
	v_cndmask_b32_e32 v3, v3, v6, vcc
	v_cndmask_b32_e32 v1, v1, v5, vcc
	v_add_u32_e32 v5, 1, v3
	v_cmp_ge_u32_e32 vcc, v1, v2
	s_nop 1
	v_cndmask_b32_e32 v1, v3, v5, vcc
	v_mad_u64_u32 v[2:3], s[6:7], v2, v1, v[2:3]
	v_cmp_ne_u32_e32 vcc, v4, v2
	v_mov_b64_e32 v[2:3], s[0:1]
	s_and_saveexec_b64 s[6:7], vcc
	s_cbranch_execz .LBB0_776
	v_mov_b64_e32 v[2:3], s[100:101]
	flat_load_dword v2, v[2:3] sc1
	s_mov_b64 s[12:13], 0
	s_waitcnt vmcnt(0) lgkmcnt(0)
	v_cmp_eq_u32_e32 vcc, v2, v1
	s_and_saveexec_b64 s[10:11], vcc
	s_cbranch_execz .LBB0_775
	s_add_u32 s8, s42, 0x4200
	s_addc_u32 s9, s43, 0
	s_mov_b32 s26, 1
	s_branch .LBB0_768

; __device__ __forceinline__ unsigned xb_ld(unsigned* p)              { return __hip_atomic_load(p, __ATOMIC_RELAXED, __HIP_MEMORY_SCOPE_AGENT); }
; __device__ __forceinline__ unsigned xb_add(unsigned* p, unsigned v) { return __hip_atomic_fetch_add(p, v, __ATOMIC_RELAXED, __HIP_MEMORY_SCOPE_AGENT); }
; #define XB_SPIN(cond, bar) do { unsigned _sp = 0; while (cond) { __builtin_amdgcn_s_sleep(1); \
;     if ((++_sp & 255u) == 0u) { if (xb_ld(&(bar)[XB_TMO])) break; if (_sp > XB_SPIN_CAP) { atomicAdd(&(bar)[XB_TMO], 1u); break; } } } } while (0)
; __device__ __forceinline__ void xcd_barrier(const XcdBarrier& b) {
;     ...
;             if (og + 1u == (tg + 1u) * nx) xb_add(&bar[XB_TOPGEN], 1u);
;             else XB_SPIN(xb_ld(&bar[XB_TOPGEN]) == tg, bar);
;             __builtin_amdgcn_fence(__ATOMIC_ACQUIRE, "agent");
;             xb_add(&bar[XB_XGEN(b.x)], 1u);
.LBB0_776:
	s_or_b64 exec, exec, s[6:7]
	s_and_saveexec_b64 s[0:1], s[8:9]
	s_cbranch_execz .LBB0_778
	v_mov_b32_e32 v1, 1
	flat_atomic_add v[2:3], v1
	v_mov_b32_e32 v4, s42
	v_add_co_u32_e32 v4, vcc, 0x6000, v4
	v_mov_b32_e32 v5, s43
	s_nop 0
	v_addc_co_u32_e32 v5, vcc, 0, v5, vcc
	flat_atomic_add v[4:5], v1 offset:1024
	flat_atomic_add v[4:5], v1 offset:1280
	flat_atomic_add v[4:5], v1 offset:1536
	flat_atomic_add v[4:5], v1 offset:1792
	flat_atomic_add v[4:5], v1 offset:2048
	flat_atomic_add v[4:5], v1 offset:2304
	flat_atomic_add v[4:5], v1 offset:2560
	flat_atomic_add v[4:5], v1 offset:2816

; __device__ __forceinline__ unsigned xb_ld(unsigned* p)              { return __hip_atomic_load(p, __ATOMIC_RELAXED, __HIP_MEMORY_SCOPE_AGENT); }
; __device__ __forceinline__ unsigned xb_add(unsigned* p, unsigned v) { return __hip_atomic_fetch_add(p, v, __ATOMIC_RELAXED, __HIP_MEMORY_SCOPE_AGENT); }
; #define XB_SPIN(cond, bar) do { unsigned _sp = 0; while (cond) { __builtin_amdgcn_s_sleep(1); \
;     if ((++_sp & 255u) == 0u) { if (xb_ld(&(bar)[XB_TMO])) break; if (_sp > XB_SPIN_CAP) { atomicAdd(&(bar)[XB_TMO], 1u); break; } } } } while (0)
; __device__ __forceinline__ void xcd_barrier(const XcdBarrier& b) {
;     ...
;         const unsigned old = xb_add(&bar[XB_XSUB(b.x)], 1u);
;         const unsigned gen = old / nloc;
;         if (old + 1u == (gen + 1u) * nloc) {
;             __builtin_amdgcn_fence(__ATOMIC_RELEASE, "agent");
;             asm volatile("s_waitcnt vmcnt(0)" ::: "memory");
;             const unsigned og = xb_add(&bar[XB_TOP], 1u);
;             const unsigned tg = og / nx;
;             if (og + 1u == (tg + 1u) * nx) xb_add(&bar[XB_TOPGEN], 1u);
;             else XB_SPIN(xb_ld(&bar[XB_TOPGEN]) == tg, bar);
.LBB0_1421:
	s_andn2_saveexec_b64 s[4:5], s[0:1]
	s_cbranch_execz .LBB0_1437
	v_mov_b32_e32 v1, s48
	v_add_co_u32_e32 v4, vcc, 0x7000, v1
	v_mov_b32_e32 v1, s49
	buffer_wbl2 sc1
	s_waitcnt vmcnt(0)
	v_addc_co_u32_e32 v5, vcc, 0, v1, vcc
	v_mov_b32_e32 v1, 1
	flat_atomic_add v1, v[4:5], v1 offset:1024 sc0
	v_cvt_f32_u32_e32 v3, v2
	v_sub_u32_e32 v4, 0, v2
	s_add_u32 s0, s48, 0x7500
	s_addc_u32 s1, s49, 0
	s_add_u32 s100, s25, 0x2400
	s_addc_u32 s101, s24, 0
	v_rcp_iflag_f32_e32 v3, v3
	s_mov_b64 s[8:9], -1
	v_mul_f32_e32 v3, 0x4f7ffffe, v3
	v_cvt_u32_f32_e32 v3, v3
	v_mul_lo_u32 v4, v4, v3
	v_mul_hi_u32 v4, v3, v4
	v_add_u32_e32 v3, v3, v4
	s_waitcnt vmcnt(0) lgkmcnt(0)
	v_mul_hi_u32 v3, v1, v3
	v_mul_lo_u32 v5, v3, v2
	v_add_u32_e32 v4, 1, v1
	v_sub_u32_e32 v1, v1, v5
	v_add_u32_e32 v6, 1, v3
	v_cmp_ge_u32_e32 vcc, v1, v2
	v_sub_u32_e32 v5, v1, v2
	s_nop 0
	v_cndmask_b32_e32 v3, v3, v6, vcc
	v_cndmask_b32_e32 v1, v1, v5, vcc
	v_add_u32_e32 v5, 1, v3
	v_cmp_ge_u32_e32 vcc, v1, v2
	s_nop 1
	v_cndmask_b32_e32 v1, v3, v5, vcc
	v_mad_u64_u32 v[2:3], s[6:7], v2, v1, v[2:3]
	v_cmp_ne_u32_e32 vcc, v4, v2
	v_mov_b64_e32 v[2:3], s[0:1]
	s_and_saveexec_b64 s[6:7], vcc
	s_cbranch_execz .LBB0_1434
	v_mov_b64_e32 v[2:3], s[100:101]
	flat_load_dword v2, v[2:3] sc1
	s_mov_b64 s[12:13], 0
	s_waitcnt vmcnt(0) lgkmcnt(0)
	v_cmp_eq_u32_e32 vcc, v2, v1
	s_and_saveexec_b64 s[10:11], vcc
	s_cbranch_execz .LBB0_1433
	s_add_u32 s8, s48, 0x4200
	s_addc_u32 s9, s49, 0
	s_mov_b32 s26, 1
	s_branch .LBB0_1426

; __device__ __forceinline__ unsigned xb_ld(unsigned* p)              { return __hip_atomic_load(p, __ATOMIC_RELAXED, __HIP_MEMORY_SCOPE_AGENT); }
; __device__ __forceinline__ unsigned xb_add(unsigned* p, unsigned v) { return __hip_atomic_fetch_add(p, v, __ATOMIC_RELAXED, __HIP_MEMORY_SCOPE_AGENT); }
; #define XB_SPIN(cond, bar) do { unsigned _sp = 0; while (cond) { __builtin_amdgcn_s_sleep(1); \
;     if ((++_sp & 255u) == 0u) { if (xb_ld(&(bar)[XB_TMO])) break; if (_sp > XB_SPIN_CAP) { atomicAdd(&(bar)[XB_TMO], 1u); break; } } } } while (0)
; __device__ __forceinline__ void xcd_barrier(const XcdBarrier& b) {
;     ...
;             if (og + 1u == (tg + 1u) * nx) xb_add(&bar[XB_TOPGEN], 1u);
;             else XB_SPIN(xb_ld(&bar[XB_TOPGEN]) == tg, bar);
;             __builtin_amdgcn_fence(__ATOMIC_ACQUIRE, "agent");
;             xb_add(&bar[XB_XGEN(b.x)], 1u);
.LBB0_1434:
	s_or_b64 exec, exec, s[6:7]
	s_and_saveexec_b64 s[0:1], s[8:9]
	s_cbranch_execz .LBB0_1436
	v_mov_b32_e32 v1, 1
	flat_atomic_add v[2:3], v1
	v_mov_b32_e32 v4, s48
	v_add_co_u32_e32 v4, vcc, 0x6000, v4
	v_mov_b32_e32 v5, s49
	s_nop 0
	v_addc_co_u32_e32 v5, vcc, 0, v5, vcc
	flat_atomic_add v[4:5], v1 offset:1024
	flat_atomic_add v[4:5], v1 offset:1280
	flat_atomic_add v[4:5], v1 offset:1536
	flat_atomic_add v[4:5], v1 offset:1792
	flat_atomic_add v[4:5], v1 offset:2048
	flat_atomic_add v[4:5], v1 offset:2304
	flat_atomic_add v[4:5], v1 offset:2560
	flat_atomic_add v[4:5], v1 offset:2816

; __device__ __forceinline__ unsigned xb_ld(unsigned* p)              { return __hip_atomic_load(p, __ATOMIC_RELAXED, __HIP_MEMORY_SCOPE_AGENT); }
; __device__ __forceinline__ unsigned xb_add(unsigned* p, unsigned v) { return __hip_atomic_fetch_add(p, v, __ATOMIC_RELAXED, __HIP_MEMORY_SCOPE_AGENT); }
; #define XB_SPIN(cond, bar) do { unsigned _sp = 0; while (cond) { __builtin_amdgcn_s_sleep(1); \
;     if ((++_sp & 255u) == 0u) { if (xb_ld(&(bar)[XB_TMO])) break; if (_sp > XB_SPIN_CAP) { atomicAdd(&(bar)[XB_TMO], 1u); break; } } } } while (0)
; __device__ __forceinline__ void xcd_barrier(const XcdBarrier& b) {
;     ...
;         const unsigned old = xb_add(&bar[XB_XSUB(b.x)], 1u);
;         const unsigned gen = old / nloc;
;         if (old + 1u == (gen + 1u) * nloc) {
;             __builtin_amdgcn_fence(__ATOMIC_RELEASE, "agent");
;             asm volatile("s_waitcnt vmcnt(0)" ::: "memory");
;             const unsigned og = xb_add(&bar[XB_TOP], 1u);
;             const unsigned tg = og / nx;
;             if (og + 1u == (tg + 1u) * nx) xb_add(&bar[XB_TOPGEN], 1u);
;             else XB_SPIN(xb_ld(&bar[XB_TOPGEN]) == tg, bar);
.LBB0_1480:
	s_andn2_saveexec_b64 s[4:5], s[0:1]
	s_cbranch_execz .LBB0_1496
	v_mov_b32_e32 v1, s33
	v_add_co_u32_e32 v4, vcc, 0x7000, v1
	v_mov_b32_e32 v1, s40
	buffer_wbl2 sc1
	s_waitcnt vmcnt(0)
	v_addc_co_u32_e32 v5, vcc, 0, v1, vcc
	v_mov_b32_e32 v1, 1
	flat_atomic_add v1, v[4:5], v1 offset:1024 sc0
	v_cvt_f32_u32_e32 v3, v2
	v_sub_u32_e32 v4, 0, v2
	s_add_u32 s0, s33, 0x7500
	s_addc_u32 s1, s40, 0
	s_add_u32 s100, s25, 0x2400
	s_addc_u32 s101, s24, 0
	v_rcp_iflag_f32_e32 v3, v3
	s_mov_b64 s[8:9], -1
	v_mul_f32_e32 v3, 0x4f7ffffe, v3
	v_cvt_u32_f32_e32 v3, v3
	v_mul_lo_u32 v4, v4, v3
	v_mul_hi_u32 v4, v3, v4
	v_add_u32_e32 v3, v3, v4
	s_waitcnt vmcnt(0) lgkmcnt(0)
	v_mul_hi_u32 v3, v1, v3
	v_mul_lo_u32 v5, v3, v2
	v_add_u32_e32 v4, 1, v1
	v_sub_u32_e32 v1, v1, v5
	v_add_u32_e32 v6, 1, v3
	v_cmp_ge_u32_e32 vcc, v1, v2
	v_sub_u32_e32 v5, v1, v2
	s_nop 0
	v_cndmask_b32_e32 v3, v3, v6, vcc
	v_cndmask_b32_e32 v1, v1, v5, vcc
	v_add_u32_e32 v5, 1, v3
	v_cmp_ge_u32_e32 vcc, v1, v2
	s_nop 1
	v_cndmask_b32_e32 v1, v3, v5, vcc
	v_mad_u64_u32 v[2:3], s[6:7], v2, v1, v[2:3]
	v_cmp_ne_u32_e32 vcc, v4, v2
	v_mov_b64_e32 v[2:3], s[0:1]
	s_and_saveexec_b64 s[6:7], vcc
	s_cbranch_execz .LBB0_1493
	v_mov_b64_e32 v[2:3], s[100:101]
	flat_load_dword v2, v[2:3] sc1
	s_mov_b64 s[12:13], 0
	s_waitcnt vmcnt(0) lgkmcnt(0)
	v_cmp_eq_u32_e32 vcc, v2, v1
	s_and_saveexec_b64 s[10:11], vcc
	s_cbranch_execz .LBB0_1492
	s_add_u32 s8, s33, 0x4200
	s_addc_u32 s9, s40, 0
	s_mov_b32 s26, 1
	s_branch .LBB0_1485

; __device__ __forceinline__ unsigned xb_ld(unsigned* p)              { return __hip_atomic_load(p, __ATOMIC_RELAXED, __HIP_MEMORY_SCOPE_AGENT); }
; __device__ __forceinline__ unsigned xb_add(unsigned* p, unsigned v) { return __hip_atomic_fetch_add(p, v, __ATOMIC_RELAXED, __HIP_MEMORY_SCOPE_AGENT); }
; #define XB_SPIN(cond, bar) do { unsigned _sp = 0; while (cond) { __builtin_amdgcn_s_sleep(1); \
;     if ((++_sp & 255u) == 0u) { if (xb_ld(&(bar)[XB_TMO])) break; if (_sp > XB_SPIN_CAP) { atomicAdd(&(bar)[XB_TMO], 1u); break; } } } } while (0)
; __device__ __forceinline__ void xcd_barrier(const XcdBarrier& b) {
;     ...
;             if (og + 1u == (tg + 1u) * nx) xb_add(&bar[XB_TOPGEN], 1u);
;             else XB_SPIN(xb_ld(&bar[XB_TOPGEN]) == tg, bar);
;             __builtin_amdgcn_fence(__ATOMIC_ACQUIRE, "agent");
;             xb_add(&bar[XB_XGEN(b.x)], 1u);
.LBB0_1493:
	s_or_b64 exec, exec, s[6:7]
	s_and_saveexec_b64 s[0:1], s[8:9]
	s_cbranch_execz .LBB0_1495
	v_mov_b32_e32 v1, 1
	flat_atomic_add v[2:3], v1
	v_mov_b32_e32 v4, s33
	v_add_co_u32_e32 v4, vcc, 0x6000, v4
	v_mov_b32_e32 v5, s40
	s_nop 0
	v_addc_co_u32_e32 v5, vcc, 0, v5, vcc
	flat_atomic_add v[4:5], v1 offset:1024
	flat_atomic_add v[4:5], v1 offset:1280
	flat_atomic_add v[4:5], v1 offset:1536
	flat_atomic_add v[4:5], v1 offset:1792
	flat_atomic_add v[4:5], v1 offset:2048
	flat_atomic_add v[4:5], v1 offset:2304
	flat_atomic_add v[4:5], v1 offset:2560
	flat_atomic_add v[4:5], v1 offset:2816

; __device__ __forceinline__ unsigned xb_ld(unsigned* p)              { return __hip_atomic_load(p, __ATOMIC_RELAXED, __HIP_MEMORY_SCOPE_AGENT); }
; __device__ __forceinline__ unsigned xb_add(unsigned* p, unsigned v) { return __hip_atomic_fetch_add(p, v, __ATOMIC_RELAXED, __HIP_MEMORY_SCOPE_AGENT); }
; #define XB_SPIN(cond, bar) do { unsigned _sp = 0; while (cond) { __builtin_amdgcn_s_sleep(1); \
;     if ((++_sp & 255u) == 0u) { if (xb_ld(&(bar)[XB_TMO])) break; if (_sp > XB_SPIN_CAP) { atomicAdd(&(bar)[XB_TMO], 1u); break; } } } } while (0)
; __device__ __forceinline__ void xcd_barrier(const XcdBarrier& b) {
;     ...
;         const unsigned old = xb_add(&bar[XB_XSUB(b.x)], 1u);
;         const unsigned gen = old / nloc;
;         if (old + 1u == (gen + 1u) * nloc) {
;             __builtin_amdgcn_fence(__ATOMIC_RELEASE, "agent");
;             asm volatile("s_waitcnt vmcnt(0)" ::: "memory");
;             const unsigned og = xb_add(&bar[XB_TOP], 1u);
;             const unsigned tg = og / nx;
;             if (og + 1u == (tg + 1u) * nx) xb_add(&bar[XB_TOPGEN], 1u);
;             else XB_SPIN(xb_ld(&bar[XB_TOPGEN]) == tg, bar);
;     ...
;             XB_SPIN(xb_ld(&bar[XB_XGEN(b.x)]) == gen, bar);
.LBB0_1911:
	s_andn2_saveexec_b64 s[4:5], s[0:1]
	s_cbranch_execz .LBB0_1927
	v_mov_b32_e32 v1, s39
	v_add_co_u32_e32 v4, vcc, 0x7000, v1
	v_mov_b32_e32 v1, s42
	buffer_wbl2 sc1
	s_waitcnt vmcnt(0)
	v_addc_co_u32_e32 v5, vcc, 0, v1, vcc
	v_mov_b32_e32 v1, 1
	flat_atomic_add v1, v[4:5], v1 offset:1024 sc0
	v_cvt_f32_u32_e32 v3, v2
	v_sub_u32_e32 v4, 0, v2
	s_add_u32 s0, s39, 0x7500
	s_addc_u32 s1, s42, 0
	s_add_u32 s100, s25, 0x2400
	s_addc_u32 s101, s24, 0
	v_rcp_iflag_f32_e32 v3, v3
	s_mov_b64 s[8:9], -1
	v_mul_f32_e32 v3, 0x4f7ffffe, v3
	v_cvt_u32_f32_e32 v3, v3
	v_mul_lo_u32 v4, v4, v3
	v_mul_hi_u32 v4, v3, v4
	v_add_u32_e32 v3, v3, v4
	s_waitcnt vmcnt(0) lgkmcnt(0)
	v_mul_hi_u32 v3, v1, v3
	v_mul_lo_u32 v5, v3, v2
	v_add_u32_e32 v4, 1, v1
	v_sub_u32_e32 v1, v1, v5
	v_add_u32_e32 v6, 1, v3
	v_cmp_ge_u32_e32 vcc, v1, v2
	v_sub_u32_e32 v5, v1, v2
	s_nop 0
	v_cndmask_b32_e32 v3, v3, v6, vcc
	v_cndmask_b32_e32 v1, v1, v5, vcc
	v_add_u32_e32 v5, 1, v3
	v_cmp_ge_u32_e32 vcc, v1, v2
	s_nop 1
	v_cndmask_b32_e32 v1, v3, v5, vcc
	v_mad_u64_u32 v[2:3], s[6:7], v2, v1, v[2:3]
	v_cmp_ne_u32_e32 vcc, v4, v2
	v_mov_b64_e32 v[2:3], s[0:1]
	s_and_saveexec_b64 s[6:7], vcc
	s_cbranch_execz .LBB0_1924
	v_mov_b64_e32 v[2:3], s[100:101]
	flat_load_dword v2, v[2:3] sc1
	s_mov_b64 s[12:13], 0
	s_waitcnt vmcnt(0) lgkmcnt(0)
	v_cmp_eq_u32_e32 vcc, v2, v1
	s_and_saveexec_b64 s[10:11], vcc
	s_cbranch_execz .LBB0_1923
	s_add_u32 s8, s39, 0x4200
	s_addc_u32 s9, s42, 0
	s_mov_b32 s26, 1
	s_branch .LBB0_1916

; __device__ __forceinline__ unsigned xb_ld(unsigned* p)              { return __hip_atomic_load(p, __ATOMIC_RELAXED, __HIP_MEMORY_SCOPE_AGENT); }
; __device__ __forceinline__ unsigned xb_add(unsigned* p, unsigned v) { return __hip_atomic_fetch_add(p, v, __ATOMIC_RELAXED, __HIP_MEMORY_SCOPE_AGENT); }
; #define XB_SPIN(cond, bar) do { unsigned _sp = 0; while (cond) { __builtin_amdgcn_s_sleep(1); \
;     if ((++_sp & 255u) == 0u) { if (xb_ld(&(bar)[XB_TMO])) break; if (_sp > XB_SPIN_CAP) { atomicAdd(&(bar)[XB_TMO], 1u); break; } } } } while (0)
; __device__ __forceinline__ void xcd_barrier(const XcdBarrier& b) {
;     ...
;             const unsigned og = xb_add(&bar[XB_TOP], 1u);
;             const unsigned tg = og / nx;
;             if (og + 1u == (tg + 1u) * nx) xb_add(&bar[XB_TOPGEN], 1u);
;             else XB_SPIN(xb_ld(&bar[XB_TOPGEN]) == tg, bar);
;             __builtin_amdgcn_fence(__ATOMIC_ACQUIRE, "agent");
;             xb_add(&bar[XB_XGEN(b.x)], 1u);
;             asm volatile("s_waitcnt vmcnt(0)" ::: "memory");
.LBB0_1924:
	s_or_b64 exec, exec, s[6:7]
	s_and_saveexec_b64 s[0:1], s[8:9]
	s_cbranch_execz .LBB0_1926
	v_mov_b32_e32 v1, 1
	flat_atomic_add v[2:3], v1
	v_mov_b32_e32 v4, s39
	v_add_co_u32_e32 v4, vcc, 0x6000, v4
	v_mov_b32_e32 v5, s42
	s_nop 0
	v_addc_co_u32_e32 v5, vcc, 0, v5, vcc
	flat_atomic_add v[4:5], v1 offset:1024
	flat_atomic_add v[4:5], v1 offset:1280
	flat_atomic_add v[4:5], v1 offset:1536
	flat_atomic_add v[4:5], v1 offset:1792
	flat_atomic_add v[4:5], v1 offset:2048
	flat_atomic_add v[4:5], v1 offset:2304
	flat_atomic_add v[4:5], v1 offset:2560
	flat_atomic_add v[4:5], v1 offset:2816

; __device__ __forceinline__ unsigned xb_ld(unsigned* p)              { return __hip_atomic_load(p, __ATOMIC_RELAXED, __HIP_MEMORY_SCOPE_AGENT); }
; __device__ __forceinline__ unsigned xb_add(unsigned* p, unsigned v) { return __hip_atomic_fetch_add(p, v, __ATOMIC_RELAXED, __HIP_MEMORY_SCOPE_AGENT); }
; #define XB_SPIN(cond, bar) do { unsigned _sp = 0; while (cond) { __builtin_amdgcn_s_sleep(1); \
;     if ((++_sp & 255u) == 0u) { if (xb_ld(&(bar)[XB_TMO])) break; if (_sp > XB_SPIN_CAP) { atomicAdd(&(bar)[XB_TMO], 1u); break; } } } } while (0)
; __device__ __forceinline__ void xcd_barrier(const XcdBarrier& b) {
;     ...
;         const unsigned old = xb_add(&bar[XB_XSUB(b.x)], 1u);
;         const unsigned gen = old / nloc;
;         if (old + 1u == (gen + 1u) * nloc) {
;             __builtin_amdgcn_fence(__ATOMIC_RELEASE, "agent");
;             asm volatile("s_waitcnt vmcnt(0)" ::: "memory");
;             const unsigned og = xb_add(&bar[XB_TOP], 1u);
;             const unsigned tg = og / nx;
;             if (og + 1u == (tg + 1u) * nx) xb_add(&bar[XB_TOPGEN], 1u);
;             else XB_SPIN(xb_ld(&bar[XB_TOPGEN]) == tg, bar);
;     ...
;             XB_SPIN(xb_ld(&bar[XB_XGEN(b.x)]) == gen, bar);
.LBB0_2161:
	s_andn2_saveexec_b64 s[4:5], s[0:1]
	s_cbranch_execz .LBB0_2177
	v_mov_b32_e32 v1, s45
	v_add_co_u32_e32 v4, vcc, 0x7000, v1
	v_mov_b32_e32 v1, s46
	buffer_wbl2 sc1
	s_waitcnt vmcnt(0)
	v_addc_co_u32_e32 v5, vcc, 0, v1, vcc
	v_mov_b32_e32 v1, 1
	flat_atomic_add v1, v[4:5], v1 offset:1024 sc0
	v_cvt_f32_u32_e32 v3, v2
	v_sub_u32_e32 v4, 0, v2
	s_add_u32 s0, s45, 0x7500
	s_addc_u32 s1, s46, 0
	s_add_u32 s100, s25, 0x2400
	s_addc_u32 s101, s24, 0
	v_rcp_iflag_f32_e32 v3, v3
	s_mov_b64 s[8:9], -1
	v_mul_f32_e32 v3, 0x4f7ffffe, v3
	v_cvt_u32_f32_e32 v3, v3
	v_mul_lo_u32 v4, v4, v3
	v_mul_hi_u32 v4, v3, v4
	v_add_u32_e32 v3, v3, v4
	s_waitcnt vmcnt(0) lgkmcnt(0)
	v_mul_hi_u32 v3, v1, v3
	v_mul_lo_u32 v5, v3, v2
	v_add_u32_e32 v4, 1, v1
	v_sub_u32_e32 v1, v1, v5
	v_add_u32_e32 v6, 1, v3
	v_cmp_ge_u32_e32 vcc, v1, v2
	v_sub_u32_e32 v5, v1, v2
	s_nop 0
	v_cndmask_b32_e32 v3, v3, v6, vcc
	v_cndmask_b32_e32 v1, v1, v5, vcc
	v_add_u32_e32 v5, 1, v3
	v_cmp_ge_u32_e32 vcc, v1, v2
	s_nop 1
	v_cndmask_b32_e32 v1, v3, v5, vcc
	v_mad_u64_u32 v[2:3], s[6:7], v2, v1, v[2:3]
	v_cmp_ne_u32_e32 vcc, v4, v2
	v_mov_b64_e32 v[2:3], s[0:1]
	s_and_saveexec_b64 s[6:7], vcc
	s_cbranch_execz .LBB0_2174
	v_mov_b64_e32 v[2:3], s[100:101]
	flat_load_dword v2, v[2:3] sc1
	s_mov_b64 s[12:13], 0
	s_waitcnt vmcnt(0) lgkmcnt(0)
	v_cmp_eq_u32_e32 vcc, v2, v1
	s_and_saveexec_b64 s[10:11], vcc
	s_cbranch_execz .LBB0_2173
	s_add_u32 s8, s45, 0x4200
	s_addc_u32 s9, s46, 0
	s_mov_b32 s26, 1
	s_branch .LBB0_2166

; __device__ __forceinline__ unsigned xb_ld(unsigned* p)              { return __hip_atomic_load(p, __ATOMIC_RELAXED, __HIP_MEMORY_SCOPE_AGENT); }
; __device__ __forceinline__ unsigned xb_add(unsigned* p, unsigned v) { return __hip_atomic_fetch_add(p, v, __ATOMIC_RELAXED, __HIP_MEMORY_SCOPE_AGENT); }
; #define XB_SPIN(cond, bar) do { unsigned _sp = 0; while (cond) { __builtin_amdgcn_s_sleep(1); \
;     if ((++_sp & 255u) == 0u) { if (xb_ld(&(bar)[XB_TMO])) break; if (_sp > XB_SPIN_CAP) { atomicAdd(&(bar)[XB_TMO], 1u); break; } } } } while (0)
; __device__ __forceinline__ void xcd_barrier(const XcdBarrier& b) {
;     ...
;             const unsigned og = xb_add(&bar[XB_TOP], 1u);
;             const unsigned tg = og / nx;
;             if (og + 1u == (tg + 1u) * nx) xb_add(&bar[XB_TOPGEN], 1u);
;             else XB_SPIN(xb_ld(&bar[XB_TOPGEN]) == tg, bar);
;             __builtin_amdgcn_fence(__ATOMIC_ACQUIRE, "agent");
;             xb_add(&bar[XB_XGEN(b.x)], 1u);
;             asm volatile("s_waitcnt vmcnt(0)" ::: "memory");
.LBB0_2174:
	s_or_b64 exec, exec, s[6:7]
	s_and_saveexec_b64 s[0:1], s[8:9]
	s_cbranch_execz .LBB0_2176
	v_mov_b32_e32 v1, 1
	flat_atomic_add v[2:3], v1
	v_mov_b32_e32 v4, s45
	v_add_co_u32_e32 v4, vcc, 0x6000, v4
	v_mov_b32_e32 v5, s46
	s_nop 0
	v_addc_co_u32_e32 v5, vcc, 0, v5, vcc
	flat_atomic_add v[4:5], v1 offset:1024
	flat_atomic_add v[4:5], v1 offset:1280
	flat_atomic_add v[4:5], v1 offset:1536
	flat_atomic_add v[4:5], v1 offset:1792
	flat_atomic_add v[4:5], v1 offset:2048
	flat_atomic_add v[4:5], v1 offset:2304
	flat_atomic_add v[4:5], v1 offset:2560
	flat_atomic_add v[4:5], v1 offset:2816
